# younger-half static priority also in phase C (rope/vT/prep) and the router phase
# baseline (speedup 1.0000x reference)
; #define IN(k) (((PHMASK >> PHBIT(k)) & 1u) && lo <= (k) && (k) < hi)
; #define SEAM(k) do { if (IN(k) && IN((k) + 1)) xcd_barrier(bar); } while (0)
; #define DUP(bit) if constexpr (((PROBE_DUP >> (bit)) & 1u) != 0u)
; __global__ void __launch_bounds__(NTHR, 2) mk_fwd(ArgsV argsv) {
;     ...
;         if (IN(pb + 2)) { { PH_BEGIN(); phase_rope(a, gw, NGW, lane); } { PH_BEGIN(); phase_vt(a, gw, NGW, lane); } DUP(PB_VT) { PH_BEGIN(); phase_vt(a, gw, NGW, lane); }
;             { PH_BEGIN(); phase_rwkvprep(a, l, lds, tid, gw, NGW, lane); } DUP(PB_RWKVPREP) { PH_BEGIN(); phase_rwkvprep(a, l, lds, tid, gw, NGW, lane); } } SEAM(pb + 2);
.LBB0_784:
	v_readfirstlane_b32 s73, v0
	s_cmpk_lt_u32 s73, 0x100
	s_cbranch_scc1 .Lprio_pc
	s_setprio 1
